# sel inner tile: K ds_read_b128 issued before the per-tile setup VALU so LDS latency overlaps it
# speedup vs baseline: 1.0067x; 1.0067x over previous
; __device__ __forceinline__ unsigned lds_addr(const LAS void* p) { return (unsigned)(size_t)p; }
; #define RD16(dst, base, off) asm volatile("ds_read_b128 %0, %1 offset:%2" : "=&v"(dst) : "v"(base), "i"(off) : "memory")
; #define LGKM_W(n) asm volatile("s_waitcnt lgkmcnt(" #n ")" ::: "memory"); SBAR()
; #define QK8_MM(T_) do { i32x8a kf; kf.lo = lo[T_]; kf.hi = hi[T_]; s[T_] = __builtin_amdgcn_mfma_scale_f32_16x16x128_f8f6f4(kf, g.q8, (f32x4){c0, c0, c0, c0}, 0, 0, 0, 0x7f7f7f7f, 0, 0x7c7c7c7c); } while (0)
; #define PV8_RD(dt) do { RD8(f.a[dt][0], vb, (dt) * 16 * VT8ST); RD8(f.a[dt][1], vb, (dt) * 16 * VT8ST + 32); } while (0)
; __device__ __forceinline__ void qk8_tile_c(f32x4 (&s)[4], const GS8& g, const unsigned kb  , const float c0  ) {
;     i32x4a lo[4], hi[4];
;     RD16(lo[0], kb, 0); RD16(hi[0], kb, 16); RD16(lo[1], kb, 16 * K8ST); RD16(hi[1], kb, 16 * K8ST + 16);
;     RD16(lo[2], kb, 32 * K8ST); RD16(hi[2], kb, 32 * K8ST + 16); RD16(lo[3], kb, 48 * K8ST); RD16(hi[3], kb, 48 * K8ST + 16);
;     ...
;     LGKM_W(6); QK8_MM(0); LGKM_W(4); QK8_MM(1); LGKM_W(2); QK8_MM(2); LGKM_W(0); QK8_MM(3);
;     ...
; }
; __device__ __forceinline__ void pv8_issue(VT8Frag& f, const unsigned vb  ) {
;     ...
;     PV8_RD(0); PV8_RD(1); PV8_RD(2); PV8_RD(3); PV8_RD(4); PV8_RD(5); PV8_RD(6); PV8_RD(7);
; template <bool DUMMY> __device__ __forceinline__ void sel_phase(Frame& F) {
;     ...
;                 const int kb = jc * 64; const bool diag = (jc == cur); f32x4 s0[4], s1[4];
;                 const float bA = selA ? 0.f : NINF, bB = selB ? 0.f : NINF;
;                 if (a0 != 0u) {
;                     const float rf = sm8_ref(g0);
;                     VT8Frag vf; qk8_tile_c(s0, g0, lds_addr(sb) + (unsigned)klane, bA + (5.f - rf)); pv8_issue(vf, lds_addr(sb + K8TB) + (unsigned)vtlane);
;                     if (diag) mask_scores(s0, tokA, 0x40000000u, kb, kq);
;                     online_sm8(s0, g0, rf);
;                     pv8_mm(g0, s0, vf);
.LBB0_1801:
	s_andn2_b64 vcc, exec, s[12:13]
	s_cbranch_vccnz .LBB0_1798
	s_lshr_b32 s45, s67, s36
	s_and_b32 s97, s45, 0xff
	s_cmp_eq_u32 s97, 0
	s_cbranch_scc1 .LBB0_1798
	s_lshr_b32 s12, s66, s36
	s_and_b32 s12, s12, 0xff
	s_and_b32 vcc_lo, s45, 15
	s_lshl_b32 s44, s12, 6
	s_cmp_eq_u32 s12, s58
	s_cselect_b64 s[12:13], -1, 0
	v_cndmask_b32_e64 v18, 0, 1, s[12:13]
	s_cmp_eq_u32 vcc_lo, 0
	v_cmp_ne_u32_e64 s[12:13], 1, v18
	s_cbranch_scc1 .LBB0_1809
	ds_read_b128 v[84:87], v208 offset:0
	ds_read_b128 v[88:91], v208 offset:16
	ds_read_b128 v[92:95], v208 offset:0x900
	ds_read_b128 v[96:99], v208 offset:0x910
	ds_read_b128 v[118:121], v208 offset:0x1200
	ds_read_b128 v[122:125], v208 offset:0x1210
	ds_read_b128 v[126:129], v208 offset:0x1b00
	ds_read_b128 v[130:133], v208 offset:0x1b10
	v_and_b32_e32 v18, s45, v154
	v_cmp_eq_u32_e32 vcc, 0, v18
	s_nop 1
	v_cndmask_b32_e32 v18, 0, v181, vcc
	v_cmp_ngt_f32_e32 vcc, s90, v19
	s_nop 1
	v_cndmask_b32_e32 v116, 0, v19, vcc
	v_sub_f32_e32 v114, 0x40a00000, v116
	v_add_f32_e32 v210, v114, v18
	s_waitcnt lgkmcnt(6)
	v_mov_b32_e32 v211, v210
	v_mov_b32_e32 v212, v210
	v_mov_b32_e32 v213, v210
	s_waitcnt lgkmcnt(4)
	s_nop 1
	v_mfma_scale_f32_16x16x128_f8f6f4 v[84:87], v[84:91], v[0:7], v[210:213], v178, v177 op_sel_hi:[0,0,0]
	v_mfma_scale_f32_16x16x128_f8f6f4 v[88:91], v[92:99], v[0:7], v[210:213], v178, v177 op_sel_hi:[0,0,0]
	s_waitcnt lgkmcnt(2)
	v_mfma_scale_f32_16x16x128_f8f6f4 v[92:95], v[118:125], v[0:7], v[210:213], v178, v177 op_sel_hi:[0,0,0]
	s_waitcnt lgkmcnt(0)
	ds_read_b64 v[148:149], v207 offset:0
	ds_read_b64 v[146:147], v207 offset:32
	ds_read_b64 v[144:145], v207 offset:0x500
	ds_read_b64 v[142:143], v207 offset:0x520
	ds_read_b64 v[140:141], v207 offset:0xa00
	ds_read_b64 v[136:137], v207 offset:0xa20
	ds_read_b64 v[138:139], v207 offset:0xf00
	ds_read_b64 v[134:135], v207 offset:0xf20
	v_mfma_scale_f32_16x16x128_f8f6f4 v[96:99], v[126:133], v[0:7], v[210:213], v178, v177 op_sel_hi:[0,0,0]
	ds_read_b64 v[132:133], v207 offset:0x1400
	ds_read_b64 v[130:131], v207 offset:0x1420
	ds_read_b64 v[128:129], v207 offset:0x1900
	ds_read_b64 v[126:127], v207 offset:0x1920
	ds_read_b64 v[124:125], v207 offset:0x1e00
	ds_read_b64 v[120:121], v207 offset:0x1e20
	ds_read_b64 v[118:119], v207 offset:0x2300
	ds_read_b64 v[122:123], v207 offset:0x2320
	s_and_b64 vcc, exec, s[12:13]
	s_cbranch_vccnz .LBB0_1806
	v_add_u32_e32 v18, s44, v155
	v_sub_u32_e32 v114, s55, v18
	v_cmp_gt_u32_e32 vcc, 2.0, v114
	v_sub_u32_e32 v114, v18, v16
	s_nop 2
	v_cndmask_b32_e32 v84, v181, v84, vcc
	v_cmp_lt_u32_e32 vcc, s91, v114
	v_sub_u32_e32 v114, v184, v18
	s_nop 0
	v_cndmask_b32_e32 v85, v181, v85, vcc
	v_cmp_gt_u32_e32 vcc, 2.0, v114
	v_sub_u32_e32 v114, v185, v18
	s_nop 0
	v_cndmask_b32_e32 v86, v181, v86, vcc
	v_cmp_gt_u32_e32 vcc, 2.0, v114
	v_sub_u32_e32 v114, s68, v18
	s_nop 0
	v_cndmask_b32_e32 v87, v181, v87, vcc
	v_cmp_gt_u32_e32 vcc, 2.0, v114
	v_sub_u32_e32 v114, v186, v18
	s_nop 0
	v_cndmask_b32_e32 v88, v181, v88, vcc
	v_cmp_gt_u32_e32 vcc, 2.0, v114
	v_sub_u32_e32 v114, v187, v18
	s_nop 0
	v_cndmask_b32_e32 v89, v181, v89, vcc
	v_cmp_gt_u32_e32 vcc, 2.0, v114
	v_sub_u32_e32 v114, v188, v18
	s_nop 0
	v_cndmask_b32_e32 v90, v181, v90, vcc
	v_cmp_gt_u32_e32 vcc, 2.0, v114
	v_sub_u32_e32 v114, s69, v18
	s_nop 0
	v_cndmask_b32_e32 v91, v181, v91, vcc
	v_cmp_gt_u32_e32 vcc, 2.0, v114
	v_sub_u32_e32 v114, v189, v18
	s_nop 0
	v_cndmask_b32_e32 v92, v181, v92, vcc
	v_cmp_gt_u32_e32 vcc, 2.0, v114
	v_sub_u32_e32 v114, v190, v18
	s_nop 0
	v_cndmask_b32_e32 v93, v181, v93, vcc
	v_cmp_gt_u32_e32 vcc, 2.0, v114
	v_sub_u32_e32 v114, v191, v18
	s_nop 0
	v_cndmask_b32_e32 v94, v181, v94, vcc
	v_cmp_gt_u32_e32 vcc, 2.0, v114
	v_sub_u32_e32 v114, s70, v18
	s_nop 0
	v_cndmask_b32_e32 v95, v181, v95, vcc
	v_cmp_gt_u32_e32 vcc, 2.0, v114
	v_sub_u32_e32 v114, v192, v18
	s_nop 0
	v_cndmask_b32_e32 v96, v181, v96, vcc
	v_cmp_gt_u32_e32 vcc, 2.0, v114
	v_sub_u32_e32 v114, v193, v18
	v_sub_u32_e32 v18, v194, v18
	v_cndmask_b32_e32 v97, v181, v97, vcc
	v_cmp_gt_u32_e32 vcc, 2.0, v114
	s_nop 1
	v_cndmask_b32_e32 v98, v181, v98, vcc
	v_cmp_gt_u32_e32 vcc, 2.0, v18
	s_nop 1
	v_cndmask_b32_e32 v99, v181, v99, vcc

; __device__ __forceinline__ unsigned lds_addr(const LAS void* p) { return (unsigned)(size_t)p; }
; #define RD16(dst, base, off) asm volatile("ds_read_b128 %0, %1 offset:%2" : "=&v"(dst) : "v"(base), "i"(off) : "memory")
; #define LGKM_W(n) asm volatile("s_waitcnt lgkmcnt(" #n ")" ::: "memory"); SBAR()
; #define QK8_MM(T_) do { i32x8a kf; kf.lo = lo[T_]; kf.hi = hi[T_]; s[T_] = __builtin_amdgcn_mfma_scale_f32_16x16x128_f8f6f4(kf, g.q8, (f32x4){c0, c0, c0, c0}, 0, 0, 0, 0x7f7f7f7f, 0, 0x7c7c7c7c); } while (0)
; #define PV8_RD(dt) do { RD8(f.a[dt][0], vb, (dt) * 16 * VT8ST); RD8(f.a[dt][1], vb, (dt) * 16 * VT8ST + 32); } while (0)
; __device__ __forceinline__ void qk8_tile_c(f32x4 (&s)[4], const GS8& g, const unsigned kb  , const float c0  ) {
;     i32x4a lo[4], hi[4];
;     RD16(lo[0], kb, 0); RD16(hi[0], kb, 16); RD16(lo[1], kb, 16 * K8ST); RD16(hi[1], kb, 16 * K8ST + 16);
;     RD16(lo[2], kb, 32 * K8ST); RD16(hi[2], kb, 32 * K8ST + 16); RD16(lo[3], kb, 48 * K8ST); RD16(hi[3], kb, 48 * K8ST + 16);
;     ...
;     LGKM_W(6); QK8_MM(0); LGKM_W(4); QK8_MM(1); LGKM_W(2); QK8_MM(2); LGKM_W(0); QK8_MM(3);
;     ...
; }
; __device__ __forceinline__ void pv8_issue(VT8Frag& f, const unsigned vb  ) {
;     ...
;     PV8_RD(0); PV8_RD(1); PV8_RD(2); PV8_RD(3); PV8_RD(4); PV8_RD(5); PV8_RD(6); PV8_RD(7);
; template <bool DUMMY> __device__ __forceinline__ void sel_phase(Frame& F) {
;     ...
;                 if (a1 != 0u) {
;                     const float rf = sm8_ref(g1);
;                     VT8Frag vf; qk8_tile_c(s0, g1, lds_addr(sb) + (unsigned)klane, bB + (5.f - rf)); pv8_issue(vf, lds_addr(sb + K8TB) + (unsigned)vtlane);
;                     if (diag) mask_scores(s0, tokA + 4, 0x40000000u, kb, kq);
;                     online_sm8(s0, g1, rf);
;                     pv8_mm(g1, s0, vf);
.LBB0_1809:
	s_cmp_lt_u32 s97, 16
	s_cbranch_scc1 .LBB0_1798
	s_lshr_b32 s45, s45, 4
	ds_read_b128 v[84:87], v208 offset:0
	ds_read_b128 v[88:91], v208 offset:16
	ds_read_b128 v[92:95], v208 offset:0x900
	ds_read_b128 v[96:99], v208 offset:0x910
	ds_read_b128 v[118:121], v208 offset:0x1200
	ds_read_b128 v[122:125], v208 offset:0x1210
	ds_read_b128 v[126:129], v208 offset:0x1b00
	ds_read_b128 v[130:133], v208 offset:0x1b10
	v_and_b32_e32 v18, s45, v154
	v_cmp_eq_u32_e32 vcc, 0, v18
	s_nop 1
	v_cndmask_b32_e32 v114, 0, v181, vcc
	v_cmp_ngt_f32_e32 vcc, s90, v117
	s_nop 1
	v_cndmask_b32_e32 v18, 0, v117, vcc
	v_sub_f32_e32 v116, 0x40a00000, v18
	v_add_f32_e32 v210, v114, v116
	s_waitcnt lgkmcnt(6)
	v_mov_b32_e32 v211, v210
	v_mov_b32_e32 v212, v210
	v_mov_b32_e32 v213, v210
	s_waitcnt lgkmcnt(4)
	s_nop 1
	v_mfma_scale_f32_16x16x128_f8f6f4 v[84:87], v[84:91], v[8:15], v[210:213], v178, v177 op_sel_hi:[0,0,0]
	v_mfma_scale_f32_16x16x128_f8f6f4 v[88:91], v[92:99], v[8:15], v[210:213], v178, v177 op_sel_hi:[0,0,0]
	s_waitcnt lgkmcnt(2)
	v_mfma_scale_f32_16x16x128_f8f6f4 v[92:95], v[118:125], v[8:15], v[210:213], v178, v177 op_sel_hi:[0,0,0]
	s_waitcnt lgkmcnt(0)
	ds_read_b64 v[148:149], v207 offset:0
	ds_read_b64 v[146:147], v207 offset:32
	ds_read_b64 v[144:145], v207 offset:0x500
	ds_read_b64 v[142:143], v207 offset:0x520
	ds_read_b64 v[140:141], v207 offset:0xa00
	ds_read_b64 v[136:137], v207 offset:0xa20
	ds_read_b64 v[138:139], v207 offset:0xf00
	ds_read_b64 v[134:135], v207 offset:0xf20
	v_mfma_scale_f32_16x16x128_f8f6f4 v[96:99], v[126:133], v[8:15], v[210:213], v178, v177 op_sel_hi:[0,0,0]
	ds_read_b64 v[132:133], v207 offset:0x1400
	ds_read_b64 v[130:131], v207 offset:0x1420
	ds_read_b64 v[128:129], v207 offset:0x1900
	ds_read_b64 v[126:127], v207 offset:0x1920
	ds_read_b64 v[124:125], v207 offset:0x1e00
	ds_read_b64 v[120:121], v207 offset:0x1e20
	ds_read_b64 v[118:119], v207 offset:0x2300
	ds_read_b64 v[122:123], v207 offset:0x2320
	s_and_b64 vcc, exec, s[12:13]
	s_cbranch_vccnz .LBB0_1812
	v_add_u32_e32 v114, s44, v155
	v_sub_u32_e32 v116, v195, v114
	v_cmp_gt_u32_e32 vcc, 2.0, v116
	v_sub_u32_e32 v116, v114, v195
	s_nop 2
	v_cndmask_b32_e32 v84, v181, v84, vcc
	v_cmp_lt_u32_e32 vcc, s91, v116
	v_sub_u32_e32 v116, v196, v114
	s_nop 0
	v_cndmask_b32_e32 v85, v181, v85, vcc
	v_cmp_gt_u32_e32 vcc, 2.0, v116
	v_sub_u32_e32 v116, v197, v114
	s_nop 0
	v_cndmask_b32_e32 v86, v181, v86, vcc
	v_cmp_gt_u32_e32 vcc, 2.0, v116
	v_sub_u32_e32 v116, s71, v114
	s_nop 0
	v_cndmask_b32_e32 v87, v181, v87, vcc
	v_cmp_gt_u32_e32 vcc, 2.0, v116
	v_sub_u32_e32 v116, v198, v114
	s_nop 0
	v_cndmask_b32_e32 v88, v181, v88, vcc
	v_cmp_gt_u32_e32 vcc, 2.0, v116
	v_sub_u32_e32 v116, v199, v114
	s_nop 0
	v_cndmask_b32_e32 v89, v181, v89, vcc
	v_cmp_gt_u32_e32 vcc, 2.0, v116
	v_sub_u32_e32 v116, v200, v114
	s_nop 0
	v_cndmask_b32_e32 v90, v181, v90, vcc
	v_cmp_gt_u32_e32 vcc, 2.0, v116
	v_sub_u32_e32 v116, s72, v114
	s_nop 0
	v_cndmask_b32_e32 v91, v181, v91, vcc
	v_cmp_gt_u32_e32 vcc, 2.0, v116
	v_sub_u32_e32 v116, v201, v114
	s_nop 0
	v_cndmask_b32_e32 v92, v181, v92, vcc
	v_cmp_gt_u32_e32 vcc, 2.0, v116
	v_sub_u32_e32 v116, v202, v114
	s_nop 0
	v_cndmask_b32_e32 v93, v181, v93, vcc
	v_cmp_gt_u32_e32 vcc, 2.0, v116
	v_sub_u32_e32 v116, v203, v114
	s_nop 0
	v_cndmask_b32_e32 v94, v181, v94, vcc
	v_cmp_gt_u32_e32 vcc, 2.0, v116
	v_sub_u32_e32 v116, s73, v114
	s_nop 0
	v_cndmask_b32_e32 v95, v181, v95, vcc
	v_cmp_gt_u32_e32 vcc, 2.0, v116
	v_sub_u32_e32 v116, v204, v114
	s_nop 0
	v_cndmask_b32_e32 v96, v181, v96, vcc
	v_cmp_gt_u32_e32 vcc, 2.0, v116
	v_sub_u32_e32 v116, v205, v114
	v_sub_u32_e32 v114, v206, v114
	v_cndmask_b32_e32 v97, v181, v97, vcc
	v_cmp_gt_u32_e32 vcc, 2.0, v116
	s_nop 1
	v_cndmask_b32_e32 v98, v181, v98, vcc
	v_cmp_gt_u32_e32 vcc, 2.0, v114
	s_nop 1
	v_cndmask_b32_e32 v99, v181, v99, vcc
